# speedup vs baseline: 1.0013x; 1.0013x over previous
_Z15k_scatter_gemm1PKiS0_PiPjPyPKfPK6__halfS5_S5_PS6_PfSA_:
	s_cmpk_gt_u32 s2, 0x186
	s_mov_b64 s[4:5], -1
	s_cbranch_scc0 .LBB1_22
	s_load_dwordx2 s[26:27], s[0:1], 0x28
	s_load_dwordx2 s[10:11], s[0:1], 0x30
	s_load_dwordx4 s[28:31], s[0:1], 0x38
	v_lshlrev_b32_e32 v92, 4, v0
	v_add_u32_e32 v93, 0x1000, v92
	v_add_u32_e32 v94, 0x2000, v92
	v_add_u32_e32 v95, 0x3000, v92
	v_add_u32_e32 v96, 0x4000, v92
	v_add_u32_e32 v97, 0x5000, v92
	v_add_u32_e32 v98, 0x6000, v92
	v_add_u32_e32 v99, 0x7000, v92
	v_add_u32_e32 v100, 0x8000, v92
	v_lshlrev_b32_e32 v101, 2, v0
	s_movk_i32 s3, 0x80
	v_cmp_gt_u32_e64 s[8:9], s3, v0
	s_waitcnt lgkmcnt(0)
	global_load_dwordx4 v[104:107], v92, s[10:11]
	global_load_dwordx4 v[108:111], v93, s[10:11]
	global_load_dwordx4 v[112:115], v94, s[10:11]
	global_load_dwordx4 v[116:119], v95, s[10:11]
	global_load_dwordx4 v[120:123], v96, s[10:11]
	global_load_dwordx4 v[124:127], v97, s[10:11]
	global_load_dwordx4 v[128:131], v98, s[10:11]
	global_load_dwordx4 v[132:135], v99, s[10:11]
	s_and_saveexec_b64 s[4:5], s[8:9]
	global_load_dwordx4 v[136:139], v100, s[10:11]
	global_load_dword v140, v101, s[28:29]
	global_load_dword v141, v101, s[30:31]
	s_mov_b64 exec, s[4:5]
	s_lshl_b32 s3, s2, 2
	v_lshrrev_b32_e32 v14, 6, v0
	s_add_i32 s4, s3, 0xfffff9e4
	v_or_b32_e32 v2, s4, v14
	s_movk_i32 s4, 2750
	v_cmp_gt_i32_e32 vcc, s4, v2
	v_and_b32_e32 v1, 15, v0
	v_and_b32_e32 v66, 48, v0
	v_mov_b32_e32 v67, 0
	s_and_saveexec_b64 s[6:7], vcc
	s_cbranch_execz .Lg1_noval
	v_lshl_or_b32 v2, v2, 4, v1
	v_ashrrev_i32_e32 v3, 31, v2
	v_lshlrev_b64 v[2:3], 9, v[2:3]
	v_lshl_add_u64 v[2:3], s[26:27], 0, v[2:3]
	v_lshl_add_u64 v[16:17], v[2:3], 0, v[66:67]
	global_load_dwordx4 v[38:41], v[16:17], off offset:448
	global_load_dwordx4 v[34:37], v[16:17], off offset:384
	global_load_dwordx4 v[46:49], v[16:17], off offset:320
	global_load_dwordx4 v[42:45], v[16:17], off offset:256
	global_load_dwordx4 v[6:9], v[16:17], off offset:192
	global_load_dwordx4 v[18:21], v[16:17], off offset:128
	global_load_dwordx4 v[2:5], v[16:17], off offset:64
	global_load_dwordx4 v[10:13], v[16:17], off
	s_mov_b64 exec, s[6:7]
	s_waitcnt vmcnt(8)
	s_branch .Lg1_stage

.Lg1_stage:
	ds_write_b128 v92, v[104:107]
	ds_write_b128 v92, v[108:111] offset:4096
	ds_write_b128 v92, v[112:115] offset:8192
	ds_write_b128 v92, v[116:119] offset:12288
	ds_write_b128 v92, v[120:123] offset:16384
	ds_write_b128 v92, v[124:127] offset:20480
	ds_write_b128 v92, v[128:131] offset:24576
	ds_write_b128 v92, v[132:135] offset:28672
	s_and_saveexec_b64 s[4:5], s[8:9]
	ds_write_b128 v92, v[136:139] offset:32768
	ds_write2st64_b32 v101, v140, v141 offset0:204 offset1:206
	s_mov_b64 exec, s[4:5]
	s_waitcnt lgkmcnt(0)
	s_barrier
	s_and_saveexec_b64 s[6:7], vcc
	s_cbranch_execz .LBB1_21
	s_load_dwordx2 s[8:9], s[0:1], 0x58
	s_load_dwordx2 s[10:11], s[0:1], 0x48
	v_and_b32_e32 v15, 63, v0
	v_lshl_add_u64 v[68:69], s[26:27], 0, v[66:67]
	s_movk_i32 s4, 0x1100
	v_cmp_gt_u32_e32 vcc, 16, v15
	v_mul_u32_u24_e32 v15, 0x110, v1
	v_mul_u32_u24_e32 v17, 0x1100, v14
	v_mad_u32_u24 v22, v14, s4, v15
	v_lshlrev_b32_e32 v16, 4, v1
	v_add_u32_e32 v25, s3, v14
	v_lshlrev_b32_e32 v14, 4, v14
	v_bfe_u32 v80, v0, 4, 2
	v_or_b32_e32 v24, v17, v16
	v_mov_b32_e32 v17, v67
	v_lshl_or_b32 v82, s2, 6, v14
	v_mbcnt_lo_u32_b32 v14, -1, 0
	s_waitcnt lgkmcnt(0)
	v_lshl_add_u64 v[70:71], s[10:11], 0, v[16:17]
	v_or_b32_e32 v17, 4, v80
	v_mbcnt_hi_u32_b32 v84, -1, v14
	v_lshlrev_b32_e32 v23, 3, v80
	v_mul_u32_u24_e32 v16, 0x110, v80
	v_mul_u32_u24_e32 v17, 0x110, v17
	v_and_b32_e32 v14, 64, v84
	v_subrev_u32_e32 v67, 56, v25
	v_or_b32_e32 v81, 0xffff9e40, v1
	s_mov_b64 s[10:11], 0
	s_movk_i32 s3, 1242
	v_add_u32_e32 v83, v66, v15
	v_xor_b32_e32 v85, 16, v84
	v_add_u32_e32 v86, 64, v14
	v_xor_b32_e32 v87, 32, v84
	v_add_u32_e32 v88, v22, v23
	v_add_u32_e32 v89, v24, v16
	v_add_u32_e32 v90, v24, v17
	s_movk_i32 s12, 1241
	s_waitcnt vmcnt(0)
	s_branch .LBB1_19

_Z12k_fine_gemm1PKjPKyPKiPiS5_S5_S5_PKfPK6__halfS7_S7_PS8_PfSC_:
	s_cmpk_gt_u32 s2, 0x186
	s_mov_b64 s[4:5], -1
	s_cbranch_scc0 .LBB2_22
	s_load_dwordx2 s[26:27], s[0:1], 0x38
	s_load_dwordx2 s[10:11], s[0:1], 0x40
	s_load_dwordx4 s[28:31], s[0:1], 0x48
	v_lshlrev_b32_e32 v92, 4, v0
	v_add_u32_e32 v93, 0x1000, v92
	v_add_u32_e32 v94, 0x2000, v92
	v_add_u32_e32 v95, 0x3000, v92
	v_add_u32_e32 v96, 0x4000, v92
	v_add_u32_e32 v97, 0x5000, v92
	v_add_u32_e32 v98, 0x6000, v92
	v_add_u32_e32 v99, 0x7000, v92
	v_add_u32_e32 v100, 0x8000, v92
	v_lshlrev_b32_e32 v101, 2, v0
	s_movk_i32 s3, 0x80
	v_cmp_gt_u32_e64 s[8:9], s3, v0
	s_waitcnt lgkmcnt(0)
	global_load_dwordx4 v[104:107], v92, s[10:11]
	global_load_dwordx4 v[108:111], v93, s[10:11]
	global_load_dwordx4 v[112:115], v94, s[10:11]
	global_load_dwordx4 v[116:119], v95, s[10:11]
	global_load_dwordx4 v[120:123], v96, s[10:11]
	global_load_dwordx4 v[124:127], v97, s[10:11]
	global_load_dwordx4 v[128:131], v98, s[10:11]
	global_load_dwordx4 v[132:135], v99, s[10:11]
	s_and_saveexec_b64 s[4:5], s[8:9]
	global_load_dwordx4 v[136:139], v100, s[10:11]
	global_load_dword v140, v101, s[28:29]
	global_load_dword v141, v101, s[30:31]
	s_mov_b64 exec, s[4:5]
	s_lshl_b32 s3, s2, 2
	v_lshrrev_b32_e32 v14, 6, v0
	s_addk_i32 s3, 1186
	v_add_u32_e32 v1, s3, v14
	s_movk_i32 s3, 0x186a
	v_cmp_gt_i32_e32 vcc, s3, v1
	v_and_b32_e32 v80, 15, v0
	v_and_b32_e32 v66, 48, v0
	v_mov_b32_e32 v67, 0
	s_and_saveexec_b64 s[6:7], vcc
	s_cbranch_execz .Lg2_noval
	v_lshl_or_b32 v2, v1, 4, v80
	v_ashrrev_i32_e32 v3, 31, v2
	v_lshlrev_b64 v[2:3], 9, v[2:3]
	v_lshl_add_u64 v[2:3], s[26:27], 0, v[2:3]
	v_lshl_add_u64 v[16:17], v[2:3], 0, v[66:67]
	global_load_dwordx4 v[38:41], v[16:17], off offset:448
	global_load_dwordx4 v[34:37], v[16:17], off offset:384
	global_load_dwordx4 v[26:29], v[16:17], off offset:320
	global_load_dwordx4 v[30:33], v[16:17], off offset:256
	global_load_dwordx4 v[6:9], v[16:17], off offset:192
	global_load_dwordx4 v[18:21], v[16:17], off offset:128
	global_load_dwordx4 v[2:5], v[16:17], off offset:64
	global_load_dwordx4 v[10:13], v[16:17], off
	s_mov_b64 exec, s[6:7]
	s_waitcnt vmcnt(8)
	s_branch .Lg2_stage

.Lg2_stage:
	ds_write_b128 v92, v[104:107]
	ds_write_b128 v92, v[108:111] offset:4096
	ds_write_b128 v92, v[112:115] offset:8192
	ds_write_b128 v92, v[116:119] offset:12288
	ds_write_b128 v92, v[120:123] offset:16384
	ds_write_b128 v92, v[124:127] offset:20480
	ds_write_b128 v92, v[128:131] offset:24576
	ds_write_b128 v92, v[132:135] offset:28672
	s_and_saveexec_b64 s[4:5], s[8:9]
	ds_write_b128 v92, v[136:139] offset:32768
	ds_write2st64_b32 v101, v140, v141 offset0:204 offset1:206
	s_mov_b64 exec, s[4:5]
	s_waitcnt lgkmcnt(0)
	s_barrier
	s_and_saveexec_b64 s[6:7], vcc
	s_cbranch_execz .LBB2_21
	s_load_dwordx2 s[8:9], s[0:1], 0x68
	s_load_dwordx2 s[10:11], s[0:1], 0x58
	v_and_b32_e32 v15, 63, v0
	s_movk_i32 s3, 0x1100
	v_cmp_gt_u32_e32 vcc, 16, v15
	v_mul_u32_u24_e32 v15, 0x110, v80
	v_mul_u32_u24_e32 v17, 0x1100, v14
	v_mad_u32_u24 v22, v14, s3, v15
	v_lshlrev_b32_e32 v16, 4, v80
	v_lshlrev_b32_e32 v14, 4, v14
	v_bfe_u32 v81, v0, 4, 2
	v_or_b32_e32 v24, v17, v16
	v_mov_b32_e32 v17, v67
	v_lshl_or_b32 v82, s2, 6, v14
	v_mbcnt_lo_u32_b32 v14, -1, 0
	s_waitcnt lgkmcnt(0)
	v_lshl_add_u64 v[70:71], s[10:11], 0, v[16:17]
	v_or_b32_e32 v17, 4, v81
	v_mbcnt_hi_u32_b32 v84, -1, v14
	v_lshlrev_b32_e32 v23, 3, v81
	v_mul_u32_u24_e32 v16, 0x110, v81
	v_mul_u32_u24_e32 v17, 0x110, v17
	v_and_b32_e32 v14, 64, v84
	v_lshl_add_u64 v[68:69], s[26:27], 0, v[66:67]
	v_or_b32_e32 v67, 0x4a20, v80
	s_mov_b64 s[10:11], 0
	s_movk_i32 s3, 0x1285
	s_movk_i32 s14, 0x1286
	v_add_u32_e32 v83, v66, v15
	v_xor_b32_e32 v85, 16, v84
	v_add_u32_e32 v86, 64, v14
	v_xor_b32_e32 v87, 32, v84
	v_add_u32_e32 v88, v22, v23
	v_add_u32_e32 v89, v24, v16
	v_add_u32_e32 v90, v24, v17
	s_waitcnt vmcnt(0)
	s_branch .LBB2_19
.LBB2_18:
	s_or_b64 exec, exec, s[12:13]
	v_cvt_pk_f16_f32 v41, v40, v41
	v_cvt_pk_f16_f32 v40, v38, v39
	v_cvt_pk_f16_f32 v38, v62, v63
	v_add_u32_e32 v62, 0x8800, v88
	v_cvt_pk_f16_f32 v37, v36, v37
	v_cvt_pk_f16_f32 v36, v34, v35
	v_cvt_pk_f16_f32 v35, v56, v57
	v_cvt_pk_f16_f32 v34, v54, v55
	ds_write2_b64 v62, v[36:37], v[34:35] offset0:8 offset1:12
	v_cvt_pk_f16_f32 v35, v48, v49
	v_cvt_pk_f16_f32 v34, v46, v47
	v_cvt_pk_f16_f32 v37, v52, v53
	v_cvt_pk_f16_f32 v36, v50, v51
	v_cvt_pk_f16_f32 v39, v64, v65
	ds_write2_b64 v62, v[34:35], v[36:37] offset0:16 offset1:20
	v_cvt_pk_f16_f32 v35, v44, v45
	v_cvt_pk_f16_f32 v34, v42, v43
	v_cvt_pk_f16_f32 v37, v60, v61
	v_cvt_pk_f16_f32 v36, v58, v59
	ds_write2_b64 v62, v[40:41], v[38:39] offset1:4
	ds_write2_b64 v62, v[34:35], v[36:37] offset0:24 offset1:28
	ds_read_b128 v[34:37], v89 offset:34816
	v_add_u32_e32 v44, v81, v82
	v_add_u32_e32 v38, 0x4a20, v44
	v_ashrrev_i32_e32 v39, 31, v38
	v_lshlrev_b64 v[38:39], 8, v[38:39]
	v_lshl_add_u64 v[42:43], v[70:71], 0, v[38:39]
	ds_read_b128 v[38:41], v90 offset:34816
	s_waitcnt lgkmcnt(1)
	global_store_dwordx4 v[42:43], v[34:37], off
	s_and_b64 s[4:5], exec, s[4:5]
	s_or_b64 s[10:11], s[4:5], s[10:11]
	v_add_u32_e32 v34, 0x4a24, v44
	v_ashrrev_i32_e32 v35, 31, v34
	v_lshlrev_b64 v[34:35], 8, v[34:35]
	v_lshl_add_u64 v[34:35], v[70:71], 0, v[34:35]
	s_waitcnt lgkmcnt(0)
	global_store_dwordx4 v[34:35], v[38:41], off
	ds_read_b128 v[34:37], v90 offset:35904
	v_add_u32_e32 v82, 0x5e40, v82
	v_add_u32_e32 v38, 0x4a28, v44
	v_ashrrev_i32_e32 v39, 31, v38
	v_lshlrev_b64 v[38:39], 8, v[38:39]
	v_lshl_add_u64 v[42:43], v[70:71], 0, v[38:39]
	ds_read_b128 v[38:41], v90 offset:36992
	s_waitcnt lgkmcnt(1)
	global_store_dwordx4 v[42:43], v[34:37], off
	s_nop 1
	v_add_u32_e32 v34, 0x4a2c, v44
	v_ashrrev_i32_e32 v35, 31, v34
	v_lshlrev_b64 v[34:35], 8, v[34:35]
	v_lshl_add_u64 v[34:35], v[70:71], 0, v[34:35]
	s_waitcnt lgkmcnt(0)
	global_store_dwordx4 v[34:35], v[38:41], off
	s_waitcnt vmcnt(5)
	v_mov_b64_e32 v[36:37], v[32:33]
	v_mov_b64_e32 v[34:35], v[30:31]
	v_mov_b64_e32 v[32:33], v[24:25]
	v_mov_b64_e32 v[30:31], v[22:23]
	s_waitcnt vmcnt(4)
	v_mov_b64_e32 v[40:41], v[28:29]
	v_mov_b64_e32 v[38:39], v[26:27]
	v_mov_b64_e32 v[28:29], v[16:17]
	v_mov_b64_e32 v[26:27], v[14:15]
	s_andn2_b64 exec, exec, s[10:11]
	s_cbranch_execz .LBB2_21
